# select_rows: next row's cache lines touched at the top of each row (2 dword loads, one lane per line, clamped at the diagonal), on top of v85
# baseline (speedup 1.0000x reference)
.LBB0_604:
	v_readlane_b32 s100, v253, 57
	s_nop 3
	s_add_i32 s100, s4, s100
	s_cmpk_lt_i32 s100, 0x4000
	s_cbranch_scc0 .Lsel_pf_skip
	v_readlane_b32 s101, v252, 0
	s_nop 3
	s_cmp_lg_u32 s101, 0x100
	s_cbranch_scc1 .Lsel_pf_norm
	s_xor_b32 s101, s100, 0x7ff
	s_bitcmp1_b32 s100, 11
	s_cselect_b32 s100, s101, s100
.Lsel_pf_norm:
	s_and_b32 s0, s100, 0xfff
	s_lshl_b32 s0, s0, 2
	s_mul_hi_i32 s101, s100, 0x4100
	s_mul_i32 s100, s100, 0x4100
	v_readlane_b32 s1, v253, 58
	s_nop 3
	s_add_u32 s100, s1, s100
	v_readlane_b32 s1, v253, 59
	s_nop 3
	s_addc_u32 s101, s1, s101
	v_lshlrev_b32_e32 v227, 7, v76
	v_add_u32_e32 v240, 0x2000, v227
	v_min_u32_e32 v227, s0, v227
	v_min_u32_e32 v240, s0, v240
	s_nop 1
	global_load_dword v227, v227, s[100:101]
	global_load_dword v240, v240, s[100:101]

.LBB0_1152:
	s_waitcnt vmcnt(0)
	v_mov_b32_e32 v227, 0x3b808081
	v_mov_b32_e32 v240, 0x43e00000
	v_readlane_b32 s2, v253, 55
	v_readlane_b32 s3, v253, 56
